# s17 + XCD affinity continued: pre-pass helper items (cumsum, block means) of batch x on XCD x; small_from_hn row blocks dealt by vcu
# baseline (speedup 1.0000x reference)
; __global__ void __launch_bounds__(NTHREADS, 2) mega(MArgs a) {
;     ...
;                 if (wv >= mlstm::NACT) for (int wq = blockIdx.x * (NWAVES - mlstm::NACT) + (wv - mlstm::NACT); wq < HB * 8 + HB * 64; wq += gridDim.x * (NWAVES - mlstm::NACT)) {
;                     if (wq < HB * 8) fox_cumsum_wave(wq, b0, (const float*)(ws + WS_SMALL), (float*)(ws + WS_CB));
;                     else moba_kmean_wave(wq - HB * 8, b0, (const h16*)(ws + WS_PROJ), (float*)(ws + WS_KMEAN)); }
.LBB0_922:
	s_cmp_lt_i32 s5, 4
	v_readlane_b32 s2, v254, 37
	s_cselect_b64 s[0:1], -1, 0
	s_add_i32 s2, s2, s5
	s_lshr_b32 s10, s2, 7
	s_and_b32 s11, s2, 127
	s_lshl_b32 s100, s10, 6
	s_add_i32 s100, s100, s11
	s_add_i32 s100, s100, 64
	s_lshl_b32 s101, s10, 3
	s_add_i32 s101, s101, s11
	s_add_i32 s101, s101, -64
	s_cmp_lt_u32 s11, 72
	s_cselect_b32 s101, s101, 0x7fff
	s_cmp_lt_u32 s11, 64
	s_cselect_b32 s2, s100, s101
	s_cmpk_gt_i32 s2, 0x23f
	s_cselect_b64 s[10:11], -1, 0
	s_or_b64 s[0:1], s[0:1], s[10:11]
	s_and_b64 vcc, exec, s[0:1]
	s_cbranch_vccz .LBB0_936

; #define PG8_LAS __attribute__((address_space(3)))
; __device__ __forceinline__ void small_from_hn(const h16* __restrict__ hn, const h16* __restrict__ wsm16  , const float* __restrict__ fox_bf, const float* __restrict__ ml_bi, ...
;     int tid_ = threadIdx.x; asm volatile("" : "+v"(tid_));
;     const int lane = tid_ & 63, wave = tid_ >> 6;
;     constexpr int WP = 1032;
; #pragma unroll
;     for (int q = 0; q < 4; ++q) { const int e = (q * NTHREADS + tid_) * 8, c = e >> 10, k = e & 1023;
;         *(PG8_LAS h16x8*)(L + (c * WP + k) * 2) = *(const h16x8*)(wsm16 + e); }
;     asm volatile("s_waitcnt vmcnt(0) lgkmcnt(0)" ::: "memory"); __syncthreads();
;     if (wave < 4) {
;         for (int blk = blockIdx.x; blk < TH / 64; blk += gridDim.x) {
;             const int R0 = blk * 64 + 16 * wave, i = lane & 15, gq = lane >> 4;
.LBB0_932:
	v_readlane_b32 s0, v255, 32
	s_cmp_eq_u32 s0, 1
	s_cbranch_scc0 .LBB0_1000
	v_readlane_b32 s0, v255, 31
	s_cmp_lt_u32 s0, 2
	v_readlane_b32 s0, v253, 54
	v_readlane_b32 s2, v253, 56
	v_readlane_b32 s1, v253, 55
	s_cselect_b32 s0, s0, s2
	v_readlane_b32 s2, v253, 57
	s_cselect_b32 s1, s1, s2
	v_readlane_b32 s2, v255, 42
	s_cmp_eq_u32 s2, 0
	v_readlane_b32 s2, v253, 24
	v_readlane_b32 s3, v253, 25
	s_cselect_b32 s3, s3, s1
	s_cselect_b32 s2, s2, s0
	v_readlane_b32 s0, v255, 36
	s_lshl_b32 s0, s0, 15
	v_readlane_b32 s4, v254, 2
	v_mov_b32_e32 v0, v243
	v_readlane_b32 s1, v255, 37
	v_readlane_b32 s5, v254, 3
	s_add_u32 s0, s4, s0
	s_addc_u32 s1, s5, 0
	v_lshlrev_b32_e32 v6, 3, v0
	v_ashrrev_i32_e32 v7, 31, v6
	v_lshl_add_u64 v[2:3], v[6:7], 1, s[0:1]
	global_load_dwordx4 v[2:5], v[2:3], off
	v_and_b32_e32 v1, 0x3f8, v6
	v_bfe_i32 v8, v0, 7, 22
	s_movk_i32 s4, 0x408
	v_mad_i32_i24 v7, v8, s4, v1
	v_lshl_add_u32 v7, v7, 1, 0
	v_add_u32_e32 v12, 0x1000, v6
	v_ashrrev_i32_e32 v13, 31, v12
	v_ashrrev_i32_e32 v9, 10, v12
	v_lshl_add_u64 v[12:13], v[12:13], 1, s[0:1]
	global_load_dwordx4 v[12:15], v[12:13], off
	v_mad_i32_i24 v9, v9, s4, v1
	v_lshl_add_u32 v9, v9, 1, 0
	v_add_u32_e32 v16, 0x2000, v6
	v_ashrrev_i32_e32 v17, 31, v16
	v_ashrrev_i32_e32 v10, 10, v16
	v_lshl_add_u64 v[16:17], v[16:17], 1, s[0:1]
	global_load_dwordx4 v[16:19], v[16:17], off
	v_mad_i32_i24 v10, v10, s4, v1
	v_lshl_add_u32 v10, v10, 1, 0
	v_add_u32_e32 v20, 0x3000, v6
	v_ashrrev_i32_e32 v21, 31, v20
	v_ashrrev_i32_e32 v6, 10, v20
	v_lshl_add_u64 v[20:21], v[20:21], 1, s[0:1]
	global_load_dwordx4 v[20:23], v[20:21], off
	v_mad_i32_i24 v1, v6, s4, v1
	v_lshl_add_u32 v1, v1, 1, 0
	v_readlane_b32 s0, v254, 63
	v_readlane_b32 s1, v255, 0
	s_waitcnt vmcnt(3)
	ds_write_b128 v7, v[2:5]
	s_waitcnt vmcnt(2)
	ds_write_b128 v9, v[12:15]
	s_waitcnt vmcnt(1)
	ds_write_b128 v10, v[16:19]
	s_waitcnt vmcnt(0)
	ds_write_b128 v1, v[20:23]
	v_ashrrev_i32_e32 v1, 6, v0
	s_waitcnt vmcnt(0) lgkmcnt(0)
	v_cmp_gt_i32_e32 vcc, 4, v1
	s_and_b64 s[0:1], vcc, s[0:1]
	s_waitcnt lgkmcnt(0)
	s_barrier
	s_and_saveexec_b64 s[14:15], s[0:1]
	s_cbranch_execz .LBB0_971
	v_readlane_b32 s0, v255, 36
	v_readlane_b32 s1, v255, 37
	s_lshl_b32 s28, s0, 2
	v_readlane_b32 s52, v253, 36
	s_mov_b32 s6, s0
	s_lshl_b64 s[0:1], s[28:29], 2
	v_readlane_b32 s64, v253, 48
	v_readlane_b32 s65, v253, 49
	s_add_u32 s4, s64, s0
	v_readlane_b32 s62, v253, 46
	s_addc_u32 s5, s65, s1
	v_lshlrev_b32_e32 v76, 4, v1
	v_and_b32_e32 v77, 15, v0
	v_bfe_u32 v1, v0, 4, 2
	v_readlane_b32 s63, v253, 47
	s_add_u32 s0, s62, s0
	v_lshlrev_b32_e32 v96, 4, v1
	v_mul_u32_u24_e32 v2, 0x408, v77
	s_addc_u32 s1, s63, s1
	s_lshl_b32 s28, s6, 3
	v_lshl_add_u64 v[68:69], s[2:3], 0, v[96:97]
	v_lshl_add_u32 v2, v1, 3, v2
	v_lshlrev_b32_e32 v96, 2, v77
	v_readlane_b32 s58, v253, 42
	s_lshl_b64 s[10:11], s[28:29], 2
	v_lshl_add_u32 v78, v2, 1, 0
	v_lshl_add_u64 v[2:3], s[4:5], 0, v[96:97]
	s_movk_i32 s4, 0xffd0
	v_lshl_add_u64 v[4:5], s[0:1], 0, v[96:97]
	s_movk_i32 s0, 0xffe0
	v_readlane_b32 s59, v253, 43
	s_add_u32 s10, s58, s10
	s_mov_b32 s5, -1
	s_mov_b32 s1, -1
	s_addc_u32 s11, s59, s11
	v_lshl_add_u64 v[2:3], v[2:3], 0, s[4:5]
	v_lshl_add_u64 v[4:5], v[4:5], 0, s[0:1]
	v_and_b32_e32 v0, 12, v0
	v_readlane_b32 s0, v255, 43
	v_cmp_gt_u32_e32 vcc, 12, v77
	v_lshl_add_u64 v[6:7], s[10:11], 0, v[96:97]
	v_cmp_ne_u32_e64 s[38:39], 8, v0
	v_lshl_or_b32 v79, v1, 2, s0
	v_cndmask_b32_e32 v0, v2, v4, vcc
	v_cndmask_b32_e32 v1, v3, v5, vcc
	v_cmp_gt_u32_e32 vcc, 8, v77
	v_lshl_add_u64 v[70:71], s[86:87], 0, v[96:97]
	v_readlane_b32 s4, v254, 36
	s_lshr_b32 s4, s4, 2
	v_cndmask_b32_e32 v73, v1, v7, vcc
	v_cndmask_b32_e32 v72, v0, v6, vcc
	v_readlane_b32 s53, v253, 37
	v_readlane_b32 s54, v253, 38
	v_readlane_b32 s55, v253, 39
	v_readlane_b32 s56, v253, 40
	v_readlane_b32 s57, v253, 41
	v_readlane_b32 s60, v253, 44
	v_readlane_b32 s61, v253, 45
	v_readlane_b32 s66, v253, 50
	v_readlane_b32 s67, v253, 51
	s_branch .LBB0_946
